# VQ phase: codebook-norm (acc init) loads one iteration ahead; plus conv1 pseudo-random first-round start delay, VQ wave stagger, c2 deeper weight prefetch, proj preload, conv1 hand-written epilogue
# baseline (speedup 1.0000x reference)
.LBB5_63:
	s_load_dwordx8 s[40:47], s[0:1], 0x38
	s_load_dwordx2 s[8:9], s[0:1], 0x18
	s_load_dwordx2 s[6:7], s[0:1], 0x28
	s_bfe_u32 s10, s33, 0x20006
	s_waitcnt vmcnt(0)
	v_lshlrev_b64 v[34:35], 4, v[146:147]
	s_lshl_b32 s12, s10, 11
	s_waitcnt lgkmcnt(0)
	s_mov_b32 s13, 0
	v_add_u32_e32 v99, s12, v34
	s_mov_b32 s60, s8
	s_mov_b32 s61, s9
	global_load_dwordx4 v[100:103], v99, s[60:61] offset:16
	global_load_dwordx4 v[104:107], v99, s[60:61]
	s_add_u32 s60, s60, 0x2000
	s_addc_u32 s61, s61, 0
	global_load_dwordx4 v[108:111], v99, s[60:61] offset:16
	global_load_dwordx4 v[112:115], v99, s[60:61]
	s_add_u32 s60, s60, 0x2000
	s_addc_u32 s61, s61, 0
	global_load_dwordx4 v[116:119], v99, s[60:61] offset:16
	global_load_dwordx4 v[120:123], v99, s[60:61]
	s_add_u32 s60, s60, 0x2000
	s_addc_u32 s61, s61, 0
	global_load_dwordx4 v[124:127], v99, s[60:61] offset:16
	global_load_dwordx4 v[128:131], v99, s[60:61]
	s_add_u32 s60, s60, 0x2000
	s_addc_u32 s61, s61, 0
	global_load_dwordx4 v[136:139], v99, s[60:61] offset:16
	global_load_dwordx4 v[140:143], v99, s[60:61]
	s_add_u32 s60, s60, 0x2000
	s_addc_u32 s61, s61, 0
	global_load_dwordx4 v[156:159], v99, s[60:61] offset:16
	global_load_dwordx4 v[160:163], v99, s[60:61]
	s_add_u32 s60, s60, 0x2000
	s_addc_u32 s61, s61, 0
	global_load_dwordx4 v[164:167], v99, s[60:61] offset:16
	global_load_dwordx4 v[168:171], v99, s[60:61]
	s_add_u32 s60, s60, 0x2000
	s_addc_u32 s61, s61, 0
	global_load_dwordx4 v[172:175], v99, s[60:61] offset:16
	global_load_dwordx4 v[176:179], v99, s[60:61]
	s_add_u32 s60, s60, 0x2000
	s_addc_u32 s61, s61, 0
	global_load_dwordx4 v[180:183], v99, s[60:61] offset:16
	global_load_dwordx4 v[184:187], v99, s[60:61]
	s_add_u32 s60, s60, 0x2000
	s_addc_u32 s61, s61, 0
	global_load_dwordx4 v[188:191], v99, s[60:61] offset:16
	global_load_dwordx4 v[192:195], v99, s[60:61]
	s_add_u32 s60, s60, 0x2000
	s_addc_u32 s61, s61, 0
	global_load_dwordx4 v[196:199], v99, s[60:61] offset:16
	global_load_dwordx4 v[200:203], v99, s[60:61]
	s_add_u32 s60, s60, 0x2000
	s_addc_u32 s61, s61, 0
	global_load_dwordx4 v[204:207], v99, s[60:61] offset:16
	global_load_dwordx4 v[208:211], v99, s[60:61]
	s_add_u32 s60, s60, 0x2000
	s_addc_u32 s61, s61, 0
	global_load_dwordx4 v[212:215], v99, s[60:61] offset:16
	global_load_dwordx4 v[216:219], v99, s[60:61]
	s_add_u32 s60, s60, 0x2000
	s_addc_u32 s61, s61, 0
	global_load_dwordx4 v[220:223], v99, s[60:61] offset:16
	global_load_dwordx4 v[224:227], v99, s[60:61]
	s_add_u32 s60, s60, 0x2000
	s_addc_u32 s61, s61, 0
	global_load_dwordx4 v[228:231], v99, s[60:61] offset:16
	global_load_dwordx4 v[232:235], v99, s[60:61]
	s_add_u32 s60, s60, 0x2000
	s_addc_u32 s61, s61, 0
	global_load_dwordx4 v[236:239], v99, s[60:61] offset:16
	global_load_dwordx4 v[240:243], v99, s[60:61]
	s_barrier
	s_lshr_b32 s8, s33, 2
	s_and_b32 s8, s8, 0x3fffffc0
	s_movk_i32 s9, 0x110
	v_or_b32_e32 v38, s8, v150
	v_mul_lo_u32 v39, v38, s9
	v_add_u32_e32 v132, v152, v39
	v_add_u32_e32 v133, 0x2200, v132
	v_add_u32_e32 v144, 0x11000, v132
	v_add_u32_e32 v145, 0x11000, v133
	ds_read_b128 v[40:43], v132
	ds_read_b128 v[44:47], v132 offset:16
	ds_read_b128 v[48:51], v133
	ds_read_b128 v[52:55], v133 offset:16
	v_mov_b32_e32 v75, 0
	s_lshl_b32 s50, s5, 2
	s_mov_b32 s51, s13
	v_lshl_add_u64 v[76:77], s[6:7], 0, v[34:35]
	s_lshl_b64 s[6:7], s[50:51], 11
	v_mov_b32_e32 v82, 0xff7fc99e
	s_brev_b32 s14, 35
	v_mov_b32_e32 v84, 0xff7fc99e
	v_mov_b32_e32 v86, 0xff7fc99e
	v_mov_b32_e32 v87, 0xff7fc99e
	v_mov_b32_e32 v88, 0xff7fc99e
	v_mov_b32_e32 v90, 0xff7fc99e
	v_mov_b32_e32 v91, 0xff7fc99e
	v_mov_b32_e32 v92, 0xff7fc99e
	v_mov_b32_e32 v94, 0xff7fc99e
	v_mov_b32_e32 v95, 0xff7fc99e
	v_mov_b32_e32 v97, 0xff7fc99e
	v_mov_b32_e32 v80, v75
	v_mov_b32_e32 v81, v75
	v_mov_b32_e32 v83, 0xff7fc99e
	v_mov_b32_e32 v98, 0xff7fc99e
	v_mov_b32_e32 v93, 0xff7fc99e
	v_mov_b32_e32 v89, 0xff7fc99e
	v_mov_b32_e32 v85, 0xff7fc99e
	s_mov_b32 s15, 0
	ds_read_b128 v[56:59], v132 offset:64
	ds_read_b128 v[60:63], v132 offset:80
	ds_read_b128 v[64:67], v133 offset:64
	ds_read_b128 v[68:71], v133 offset:80
	s_waitcnt vmcnt(31) lgkmcnt(7)
	v_mfma_f32_32x32x16_f16 v[18:33], v[100:103], v[40:43], 0
	s_waitcnt lgkmcnt(5)
	v_mfma_f32_32x32x16_f16 v[2:17], v[100:103], v[48:51], 0
	s_waitcnt vmcnt(30) lgkmcnt(4)
	v_mfma_f32_32x32x16_f16 v[18:33], v[104:107], v[44:47], v[18:33]
	v_mfma_f32_32x32x16_f16 v[2:17], v[104:107], v[52:55], v[2:17]
	v_mfma_f32_32x32x16_f16 v[18:33], v[104:107], v[40:43], v[18:33]
	v_mfma_f32_32x32x16_f16 v[2:17], v[104:107], v[48:51], v[2:17]
	ds_read_b128 v[40:43], v132 offset:128
	ds_read_b128 v[44:47], v132 offset:144
	ds_read_b128 v[48:51], v133 offset:128
	ds_read_b128 v[52:55], v133 offset:144
	s_waitcnt vmcnt(29) lgkmcnt(7)
	v_mfma_f32_32x32x16_f16 v[18:33], v[108:111], v[56:59], v[18:33]
	s_waitcnt lgkmcnt(5)
	v_mfma_f32_32x32x16_f16 v[2:17], v[108:111], v[64:67], v[2:17]
	s_waitcnt vmcnt(28) lgkmcnt(4)
	v_mfma_f32_32x32x16_f16 v[18:33], v[112:115], v[60:63], v[18:33]
	v_mfma_f32_32x32x16_f16 v[2:17], v[112:115], v[68:71], v[2:17]
	v_mfma_f32_32x32x16_f16 v[18:33], v[112:115], v[56:59], v[18:33]
	v_mfma_f32_32x32x16_f16 v[2:17], v[112:115], v[64:67], v[2:17]
	ds_read_b128 v[56:59], v132 offset:192
	ds_read_b128 v[60:63], v132 offset:208
	ds_read_b128 v[64:67], v133 offset:192
	ds_read_b128 v[68:71], v133 offset:208
	s_waitcnt vmcnt(27) lgkmcnt(7)
	v_mfma_f32_32x32x16_f16 v[18:33], v[116:119], v[40:43], v[18:33]
	s_waitcnt lgkmcnt(5)
	v_mfma_f32_32x32x16_f16 v[2:17], v[116:119], v[48:51], v[2:17]
	s_waitcnt vmcnt(26) lgkmcnt(4)
	v_mfma_f32_32x32x16_f16 v[18:33], v[120:123], v[44:47], v[18:33]
	v_mfma_f32_32x32x16_f16 v[2:17], v[120:123], v[52:55], v[2:17]
	v_mfma_f32_32x32x16_f16 v[18:33], v[120:123], v[40:43], v[18:33]
	v_mfma_f32_32x32x16_f16 v[2:17], v[120:123], v[48:51], v[2:17]
	ds_read_b128 v[40:43], v132 offset:34816
	ds_read_b128 v[44:47], v132 offset:34832
	ds_read_b128 v[48:51], v133 offset:34816
	ds_read_b128 v[52:55], v133 offset:34832
	s_waitcnt vmcnt(25) lgkmcnt(7)
	v_mfma_f32_32x32x16_f16 v[18:33], v[124:127], v[56:59], v[18:33]
	s_waitcnt lgkmcnt(5)
	v_mfma_f32_32x32x16_f16 v[2:17], v[124:127], v[64:67], v[2:17]
	s_waitcnt vmcnt(24) lgkmcnt(4)
	v_mfma_f32_32x32x16_f16 v[18:33], v[128:131], v[60:63], v[18:33]
	v_mfma_f32_32x32x16_f16 v[2:17], v[128:131], v[68:71], v[2:17]
	v_mfma_f32_32x32x16_f16 v[18:33], v[128:131], v[56:59], v[18:33]
	v_mfma_f32_32x32x16_f16 v[2:17], v[128:131], v[64:67], v[2:17]
	ds_read_b128 v[56:59], v132 offset:34880
	ds_read_b128 v[60:63], v132 offset:34896
	ds_read_b128 v[64:67], v133 offset:34880
	ds_read_b128 v[68:71], v133 offset:34896
	s_waitcnt vmcnt(23) lgkmcnt(7)
	v_mfma_f32_32x32x16_f16 v[18:33], v[136:139], v[40:43], v[18:33]
	s_waitcnt lgkmcnt(5)
	v_mfma_f32_32x32x16_f16 v[2:17], v[136:139], v[48:51], v[2:17]
	s_waitcnt vmcnt(22) lgkmcnt(4)
	v_mfma_f32_32x32x16_f16 v[18:33], v[140:143], v[44:47], v[18:33]
	v_mfma_f32_32x32x16_f16 v[2:17], v[140:143], v[52:55], v[2:17]
	v_mfma_f32_32x32x16_f16 v[18:33], v[140:143], v[40:43], v[18:33]
	v_mfma_f32_32x32x16_f16 v[2:17], v[140:143], v[48:51], v[2:17]
	ds_read_b128 v[40:43], v132 offset:34944
	ds_read_b128 v[44:47], v132 offset:34960
	ds_read_b128 v[48:51], v133 offset:34944
	ds_read_b128 v[52:55], v133 offset:34960
	s_waitcnt vmcnt(21) lgkmcnt(7)
	v_mfma_f32_32x32x16_f16 v[18:33], v[156:159], v[56:59], v[18:33]
	s_waitcnt lgkmcnt(5)
	v_mfma_f32_32x32x16_f16 v[2:17], v[156:159], v[64:67], v[2:17]
	s_waitcnt vmcnt(20) lgkmcnt(4)
	v_mfma_f32_32x32x16_f16 v[18:33], v[160:163], v[60:63], v[18:33]
	v_mfma_f32_32x32x16_f16 v[2:17], v[160:163], v[68:71], v[2:17]
	v_mfma_f32_32x32x16_f16 v[18:33], v[160:163], v[56:59], v[18:33]
	v_mfma_f32_32x32x16_f16 v[2:17], v[160:163], v[64:67], v[2:17]
	ds_read_b128 v[56:59], v132 offset:35008
	ds_read_b128 v[60:63], v132 offset:35024
	ds_read_b128 v[64:67], v133 offset:35008
	ds_read_b128 v[68:71], v133 offset:35024
	s_waitcnt vmcnt(19) lgkmcnt(7)
	v_mfma_f32_32x32x16_f16 v[18:33], v[164:167], v[40:43], v[18:33]
	s_waitcnt lgkmcnt(5)
	v_mfma_f32_32x32x16_f16 v[2:17], v[164:167], v[48:51], v[2:17]
	s_waitcnt vmcnt(18) lgkmcnt(4)
	v_mfma_f32_32x32x16_f16 v[18:33], v[168:171], v[44:47], v[18:33]
	v_mfma_f32_32x32x16_f16 v[2:17], v[168:171], v[52:55], v[2:17]
	v_mfma_f32_32x32x16_f16 v[18:33], v[168:171], v[40:43], v[18:33]
	v_mfma_f32_32x32x16_f16 v[2:17], v[168:171], v[48:51], v[2:17]
	ds_read_b128 v[40:43], v144
	ds_read_b128 v[44:47], v144 offset:16
	ds_read_b128 v[48:51], v145
	ds_read_b128 v[52:55], v145 offset:16
	s_waitcnt vmcnt(17) lgkmcnt(7)
	v_mfma_f32_32x32x16_f16 v[18:33], v[172:175], v[56:59], v[18:33]
	s_waitcnt lgkmcnt(5)
	v_mfma_f32_32x32x16_f16 v[2:17], v[172:175], v[64:67], v[2:17]
	s_waitcnt vmcnt(16) lgkmcnt(4)
	v_mfma_f32_32x32x16_f16 v[18:33], v[176:179], v[60:63], v[18:33]
	v_mfma_f32_32x32x16_f16 v[2:17], v[176:179], v[68:71], v[2:17]
	v_mfma_f32_32x32x16_f16 v[18:33], v[176:179], v[56:59], v[18:33]
	v_mfma_f32_32x32x16_f16 v[2:17], v[176:179], v[64:67], v[2:17]
	ds_read_b128 v[56:59], v144 offset:64
	ds_read_b128 v[60:63], v144 offset:80
	ds_read_b128 v[64:67], v145 offset:64
	ds_read_b128 v[68:71], v145 offset:80
	s_waitcnt vmcnt(15) lgkmcnt(7)
	v_mfma_f32_32x32x16_f16 v[18:33], v[180:183], v[40:43], v[18:33]
	s_waitcnt lgkmcnt(5)
	v_mfma_f32_32x32x16_f16 v[2:17], v[180:183], v[48:51], v[2:17]
	s_waitcnt vmcnt(14) lgkmcnt(4)
	v_mfma_f32_32x32x16_f16 v[18:33], v[184:187], v[44:47], v[18:33]
	v_mfma_f32_32x32x16_f16 v[2:17], v[184:187], v[52:55], v[2:17]
	v_mfma_f32_32x32x16_f16 v[18:33], v[184:187], v[40:43], v[18:33]
	v_mfma_f32_32x32x16_f16 v[2:17], v[184:187], v[48:51], v[2:17]
	ds_read_b128 v[40:43], v144 offset:128
	ds_read_b128 v[44:47], v144 offset:144
	ds_read_b128 v[48:51], v145 offset:128
	ds_read_b128 v[52:55], v145 offset:144
	s_waitcnt vmcnt(13) lgkmcnt(7)
	v_mfma_f32_32x32x16_f16 v[18:33], v[188:191], v[56:59], v[18:33]
	s_waitcnt lgkmcnt(5)
	v_mfma_f32_32x32x16_f16 v[2:17], v[188:191], v[64:67], v[2:17]
	s_waitcnt vmcnt(12) lgkmcnt(4)
	v_mfma_f32_32x32x16_f16 v[18:33], v[192:195], v[60:63], v[18:33]
	v_mfma_f32_32x32x16_f16 v[2:17], v[192:195], v[68:71], v[2:17]
	v_mfma_f32_32x32x16_f16 v[18:33], v[192:195], v[56:59], v[18:33]
	v_mfma_f32_32x32x16_f16 v[2:17], v[192:195], v[64:67], v[2:17]
	ds_read_b128 v[56:59], v144 offset:192
	ds_read_b128 v[60:63], v144 offset:208
	ds_read_b128 v[64:67], v145 offset:192
	ds_read_b128 v[68:71], v145 offset:208
	s_waitcnt vmcnt(11) lgkmcnt(7)
	v_mfma_f32_32x32x16_f16 v[18:33], v[196:199], v[40:43], v[18:33]
	s_waitcnt lgkmcnt(5)
	v_mfma_f32_32x32x16_f16 v[2:17], v[196:199], v[48:51], v[2:17]
	s_waitcnt vmcnt(10) lgkmcnt(4)
	v_mfma_f32_32x32x16_f16 v[18:33], v[200:203], v[44:47], v[18:33]
	v_mfma_f32_32x32x16_f16 v[2:17], v[200:203], v[52:55], v[2:17]
	v_mfma_f32_32x32x16_f16 v[18:33], v[200:203], v[40:43], v[18:33]
	v_mfma_f32_32x32x16_f16 v[2:17], v[200:203], v[48:51], v[2:17]
	ds_read_b128 v[40:43], v144 offset:34816
	ds_read_b128 v[44:47], v144 offset:34832
	ds_read_b128 v[48:51], v145 offset:34816
	ds_read_b128 v[52:55], v145 offset:34832
	s_waitcnt vmcnt(9) lgkmcnt(7)
	v_mfma_f32_32x32x16_f16 v[18:33], v[204:207], v[56:59], v[18:33]
	s_waitcnt lgkmcnt(5)
	v_mfma_f32_32x32x16_f16 v[2:17], v[204:207], v[64:67], v[2:17]
	s_waitcnt vmcnt(8) lgkmcnt(4)
	v_mfma_f32_32x32x16_f16 v[18:33], v[208:211], v[60:63], v[18:33]
	v_mfma_f32_32x32x16_f16 v[2:17], v[208:211], v[68:71], v[2:17]
	v_mfma_f32_32x32x16_f16 v[18:33], v[208:211], v[56:59], v[18:33]
	v_mfma_f32_32x32x16_f16 v[2:17], v[208:211], v[64:67], v[2:17]
	ds_read_b128 v[56:59], v144 offset:34880
	ds_read_b128 v[60:63], v144 offset:34896
	ds_read_b128 v[64:67], v145 offset:34880
	ds_read_b128 v[68:71], v145 offset:34896
	s_waitcnt vmcnt(7) lgkmcnt(7)
	v_mfma_f32_32x32x16_f16 v[18:33], v[212:215], v[40:43], v[18:33]
	s_waitcnt lgkmcnt(5)
	v_mfma_f32_32x32x16_f16 v[2:17], v[212:215], v[48:51], v[2:17]
	s_waitcnt vmcnt(6) lgkmcnt(4)
	v_mfma_f32_32x32x16_f16 v[18:33], v[216:219], v[44:47], v[18:33]
	v_mfma_f32_32x32x16_f16 v[2:17], v[216:219], v[52:55], v[2:17]
	v_mfma_f32_32x32x16_f16 v[18:33], v[216:219], v[40:43], v[18:33]
	v_mfma_f32_32x32x16_f16 v[2:17], v[216:219], v[48:51], v[2:17]
	ds_read_b128 v[40:43], v144 offset:34944
	ds_read_b128 v[44:47], v144 offset:34960
	ds_read_b128 v[48:51], v145 offset:34944
	ds_read_b128 v[52:55], v145 offset:34960
	s_waitcnt vmcnt(5) lgkmcnt(7)
	v_mfma_f32_32x32x16_f16 v[18:33], v[220:223], v[56:59], v[18:33]
	s_waitcnt lgkmcnt(5)
	v_mfma_f32_32x32x16_f16 v[2:17], v[220:223], v[64:67], v[2:17]
	s_waitcnt vmcnt(4) lgkmcnt(4)
	v_mfma_f32_32x32x16_f16 v[18:33], v[224:227], v[60:63], v[18:33]
	v_mfma_f32_32x32x16_f16 v[2:17], v[224:227], v[68:71], v[2:17]
	v_mfma_f32_32x32x16_f16 v[18:33], v[224:227], v[56:59], v[18:33]
	v_mfma_f32_32x32x16_f16 v[2:17], v[224:227], v[64:67], v[2:17]
	ds_read_b128 v[56:59], v144 offset:35008
	ds_read_b128 v[60:63], v144 offset:35024
	ds_read_b128 v[64:67], v145 offset:35008
	ds_read_b128 v[68:71], v145 offset:35024
	s_waitcnt vmcnt(3) lgkmcnt(7)
	v_mfma_f32_32x32x16_f16 v[18:33], v[228:231], v[40:43], v[18:33]
	s_waitcnt lgkmcnt(5)
	v_mfma_f32_32x32x16_f16 v[2:17], v[228:231], v[48:51], v[2:17]
	s_waitcnt vmcnt(2) lgkmcnt(4)
	v_mfma_f32_32x32x16_f16 v[18:33], v[232:235], v[44:47], v[18:33]
	v_mfma_f32_32x32x16_f16 v[2:17], v[232:235], v[52:55], v[2:17]
	v_mfma_f32_32x32x16_f16 v[18:33], v[232:235], v[40:43], v[18:33]
	s_lshl_b32 s8, s10, 5
	v_or_b32_e32 v74, s8, v134
	s_waitcnt vmcnt(0)
	v_lshl_add_u64 v[36:37], v[74:75], 2, s[24:25]
	s_waitcnt lgkmcnt(0)
	s_barrier
	v_add_u32_e32 v74, s8, v134
	v_mfma_f32_32x32x16_f16 v[2:17], v[232:235], v[48:51], v[2:17]
	global_load_dwordx4 v[48:51], v[36:37], off
	v_lshl_add_u64 v[36:37], v[74:75], 2, s[24:25]
	global_load_dwordx4 v[52:55], v[36:37], off offset:32
	s_mov_b32 s8, 0x3a800000
	v_mov_b32_e32 v74, v75
	s_waitcnt vmcnt(3)
	v_mfma_f32_32x32x16_f16 v[18:33], v[236:239], v[56:59], v[18:33]
	s_waitcnt vmcnt(2)
	v_mfma_f32_32x32x16_f16 v[18:33], v[240:243], v[60:63], v[18:33]
	v_lshl_add_u32 v62, s10, 7, v135
	s_mov_b32 s10, 0x41800000
	v_mov_b32_e32 v135, v75
	v_lshl_add_u64 v[78:79], v[134:135], 2, s[22:23]
	v_mfma_f32_32x32x16_f16 v[2:17], v[236:239], v[64:67], v[2:17]
	v_mfma_f32_32x32x16_f16 v[18:33], v[240:243], v[56:59], v[18:33]
	global_load_dwordx4 v[56:59], v[36:37], off offset:64
	v_mfma_f32_32x32x16_f16 v[2:17], v[240:243], v[68:71], v[2:17]
	s_waitcnt vmcnt(2)
	s_nop 8
	v_fma_f32 v18, v18, s8, v48
	v_fma_f32 v19, v19, s8, v49
	v_fma_f32 v20, v20, s8, v50
	v_fma_f32 v21, v21, s8, v51
	v_pk_mul_f32 v[60:61], v[18:19], s[10:11] op_sel_hi:[1,0]
	v_pk_mul_f32 v[46:47], v[20:21], s[10:11] op_sel_hi:[1,0]
	v_cvt_pk_f16_f32 v60, v60, v61
	v_cvt_f32_f16_e32 v44, v60
	v_cvt_f32_f16_sdwa v45, v60 dst_sel:DWORD dst_unused:UNUSED_PAD src0_sel:WORD_1
	v_mfma_f32_32x32x16_f16 v[2:17], v[240:243], v[64:67], v[2:17]
	v_cvt_pk_f16_f32 v61, v46, v47
	v_cvt_f32_f16_e32 v46, v61
	v_cvt_f32_f16_sdwa v47, v61 dst_sel:DWORD dst_unused:UNUSED_PAD src0_sel:WORD_1
	v_fma_f32 v18, v18, s10, -v44
	v_fma_f32 v19, v19, s10, -v45
	s_movk_i32 s9, 0x210
	v_cvt_pk_f16_f32 v44, v18, v19
	v_pk_fma_f32 v[18:19], v[20:21], s[10:11], v[46:47] op_sel_hi:[1,0,1] neg_lo:[0,0,1] neg_hi:[0,0,1]
	s_nop 3
	v_pk_fma_f32 v[2:3], v[2:3], s[8:9], v[48:49] op_sel_hi:[1,0,1]
	v_cvt_pk_f16_f32 v45, v18, v19
	v_pk_mul_f32 v[18:19], v[2:3], s[10:11] op_sel_hi:[1,0]
	v_mul_lo_u32 v46, v38, s9
	v_cvt_pk_f16_f32 v38, v18, v19
	global_load_dwordx4 v[18:21], v[36:37], off offset:96
	v_pk_fma_f32 v[4:5], v[4:5], s[8:9], v[50:51] op_sel_hi:[1,0,1]
	v_cvt_f32_f16_e32 v40, v38
	v_pk_mul_f32 v[36:37], v[4:5], s[10:11] op_sel_hi:[1,0]
	v_cvt_f32_f16_sdwa v41, v38 dst_sel:DWORD dst_unused:UNUSED_PAD src0_sel:WORD_1
	v_cvt_pk_f16_f32 v39, v36, v37
	v_cvt_f32_f16_e32 v36, v39
	v_cvt_f32_f16_sdwa v37, v39 dst_sel:DWORD dst_unused:UNUSED_PAD src0_sel:WORD_1
	v_pk_fma_f32 v[2:3], v[2:3], s[10:11], v[40:41] op_sel_hi:[1,0,1] neg_lo:[0,0,1] neg_hi:[0,0,1]
	v_add_u32_e32 v40, 0x4200, v46
	v_cvt_pk_f16_f32 v2, v2, v3
	v_pk_fma_f32 v[4:5], v[4:5], s[10:11], v[36:37] op_sel_hi:[1,0,1] neg_lo:[0,0,1] neg_hi:[0,0,1]
	s_waitcnt vmcnt(2)
	v_pk_fma_f32 v[24:25], v[24:25], s[8:9], v[54:55] op_sel_hi:[1,0,1]
	v_cvt_pk_f16_f32 v3, v4, v5
	v_add_u32_e32 v4, v62, v40
	ds_write2_b64 v4, v[38:39], v[2:3] offset1:2
	v_pk_fma_f32 v[2:3], v[22:23], s[8:9], v[52:53] op_sel_hi:[1,0,1]
	v_pk_mul_f32 v[36:37], v[24:25], s[10:11] op_sel_hi:[1,0]
	v_pk_mul_f32 v[4:5], v[2:3], s[10:11] op_sel_hi:[1,0]
	v_pk_fma_f32 v[6:7], v[6:7], s[8:9], v[52:53] op_sel_hi:[1,0,1]
	v_cvt_pk_f16_f32 v4, v4, v5
	v_cvt_pk_f16_f32 v5, v36, v37
	v_cvt_f32_f16_e32 v22, v4
	v_cvt_f32_f16_sdwa v23, v4 dst_sel:DWORD dst_unused:UNUSED_PAD src0_sel:WORD_1
	v_cvt_f32_f16_e32 v36, v5
	v_cvt_f32_f16_sdwa v37, v5 dst_sel:DWORD dst_unused:UNUSED_PAD src0_sel:WORD_1
	v_pk_fma_f32 v[8:9], v[8:9], s[8:9], v[54:55] op_sel_hi:[1,0,1]
	v_pk_fma_f32 v[2:3], v[2:3], s[10:11], v[22:23] op_sel_hi:[1,0,1] neg_lo:[0,0,1] neg_hi:[0,0,1]
	v_add_u32_e32 v38, 32, v62
	v_pk_fma_f32 v[22:23], v[24:25], s[10:11], v[36:37] op_sel_hi:[1,0,1] neg_lo:[0,0,1] neg_hi:[0,0,1]
	v_cvt_pk_f16_f32 v2, v2, v3
	v_cvt_pk_f16_f32 v3, v22, v23
	v_pk_mul_f32 v[22:23], v[6:7], s[10:11] op_sel_hi:[1,0]
	v_pk_mul_f32 v[36:37], v[8:9], s[10:11] op_sel_hi:[1,0]
	v_cvt_pk_f16_f32 v22, v22, v23
	v_cvt_pk_f16_f32 v23, v36, v37
	v_cvt_f32_f16_e32 v24, v22
	v_cvt_f32_f16_sdwa v25, v22 dst_sel:DWORD dst_unused:UNUSED_PAD src0_sel:WORD_1
	v_cvt_f32_f16_e32 v36, v23
	v_cvt_f32_f16_sdwa v37, v23 dst_sel:DWORD dst_unused:UNUSED_PAD src0_sel:WORD_1
	v_add_u32_e32 v39, v38, v46
	ds_write2_b64 v39, v[4:5], v[2:3] offset1:2
	v_pk_fma_f32 v[2:3], v[6:7], s[10:11], v[24:25] op_sel_hi:[1,0,1] neg_lo:[0,0,1] neg_hi:[0,0,1]
	v_pk_fma_f32 v[4:5], v[8:9], s[10:11], v[36:37] op_sel_hi:[1,0,1] neg_lo:[0,0,1] neg_hi:[0,0,1]
	v_cvt_pk_f16_f32 v2, v2, v3
	v_cvt_pk_f16_f32 v3, v4, v5
	v_add_u32_e32 v4, v38, v40
	ds_write2_b64 v4, v[22:23], v[2:3] offset1:2
	v_add_u32_e32 v24, 64, v62
	v_add_u32_e32 v25, v24, v46
	v_add_u32_e32 v47, v62, v46
	ds_write2_b64 v47, v[60:61], v[44:45] offset1:2
	s_waitcnt vmcnt(1)
	v_pk_fma_f32 v[2:3], v[26:27], s[8:9], v[56:57] op_sel_hi:[1,0,1]
	v_pk_fma_f32 v[8:9], v[28:29], s[8:9], v[58:59] op_sel_hi:[1,0,1]
	v_pk_mul_f32 v[4:5], v[2:3], s[10:11] op_sel_hi:[1,0]
	v_pk_mul_f32 v[22:23], v[8:9], s[10:11] op_sel_hi:[1,0]
	v_cvt_pk_f16_f32 v4, v4, v5
	v_cvt_pk_f16_f32 v5, v22, v23
	v_cvt_f32_f16_e32 v6, v4
	v_cvt_f32_f16_sdwa v7, v4 dst_sel:DWORD dst_unused:UNUSED_PAD src0_sel:WORD_1
	v_cvt_f32_f16_e32 v22, v5
	v_cvt_f32_f16_sdwa v23, v5 dst_sel:DWORD dst_unused:UNUSED_PAD src0_sel:WORD_1
	v_pk_fma_f32 v[12:13], v[12:13], s[8:9], v[58:59] op_sel_hi:[1,0,1]
	v_pk_fma_f32 v[2:3], v[2:3], s[10:11], v[6:7] op_sel_hi:[1,0,1] neg_lo:[0,0,1] neg_hi:[0,0,1]
	v_mad_u32_u24 v96, v150, s9, v152
	v_pk_fma_f32 v[6:7], v[8:9], s[10:11], v[22:23] op_sel_hi:[1,0,1] neg_lo:[0,0,1] neg_hi:[0,0,1]
	v_cvt_pk_f16_f32 v2, v2, v3
	v_cvt_pk_f16_f32 v3, v6, v7
	v_pk_fma_f32 v[6:7], v[10:11], s[8:9], v[56:57] op_sel_hi:[1,0,1]
	v_pk_mul_f32 v[22:23], v[12:13], s[10:11] op_sel_hi:[1,0]
	v_pk_mul_f32 v[8:9], v[6:7], s[10:11] op_sel_hi:[1,0]
	ds_write2_b64 v25, v[4:5], v[2:3] offset1:2
	v_cvt_pk_f16_f32 v8, v8, v9
	v_cvt_pk_f16_f32 v9, v22, v23
	v_cvt_f32_f16_e32 v10, v8
	v_cvt_f32_f16_sdwa v11, v8 dst_sel:DWORD dst_unused:UNUSED_PAD src0_sel:WORD_1
	v_cvt_f32_f16_e32 v22, v9
	v_cvt_f32_f16_sdwa v23, v9 dst_sel:DWORD dst_unused:UNUSED_PAD src0_sel:WORD_1
	v_pk_fma_f32 v[2:3], v[6:7], s[10:11], v[10:11] op_sel_hi:[1,0,1] neg_lo:[0,0,1] neg_hi:[0,0,1]
	s_nop 0
	v_cvt_pk_f16_f32 v2, v2, v3
	v_pk_fma_f32 v[4:5], v[12:13], s[10:11], v[22:23] op_sel_hi:[1,0,1] neg_lo:[0,0,1] neg_hi:[0,0,1]
	s_waitcnt vmcnt(0)
	v_pk_fma_f32 v[12:13], v[16:17], s[8:9], v[20:21] op_sel_hi:[1,0,1]
	v_cvt_pk_f16_f32 v3, v4, v5
	v_add_u32_e32 v4, v24, v40
	ds_write2_b64 v4, v[8:9], v[2:3] offset1:2
	v_pk_fma_f32 v[2:3], v[30:31], s[8:9], v[18:19] op_sel_hi:[1,0,1]
	v_pk_fma_f32 v[8:9], v[32:33], s[8:9], v[20:21] op_sel_hi:[1,0,1]
	v_pk_mul_f32 v[4:5], v[2:3], s[10:11] op_sel_hi:[1,0]
	v_pk_mul_f32 v[10:11], v[8:9], s[10:11] op_sel_hi:[1,0]
	v_cvt_pk_f16_f32 v4, v4, v5
	v_cvt_pk_f16_f32 v5, v10, v11
	v_cvt_f32_f16_e32 v6, v4
	v_cvt_f32_f16_sdwa v7, v4 dst_sel:DWORD dst_unused:UNUSED_PAD src0_sel:WORD_1
	v_cvt_f32_f16_e32 v10, v5
	v_cvt_f32_f16_sdwa v11, v5 dst_sel:DWORD dst_unused:UNUSED_PAD src0_sel:WORD_1
	v_add_u32_e32 v22, 0x60, v62
	v_pk_fma_f32 v[2:3], v[2:3], s[10:11], v[6:7] op_sel_hi:[1,0,1] neg_lo:[0,0,1] neg_hi:[0,0,1]
	v_add_u32_e32 v23, v22, v46
	v_pk_fma_f32 v[6:7], v[8:9], s[10:11], v[10:11] op_sel_hi:[1,0,1] neg_lo:[0,0,1] neg_hi:[0,0,1]
	v_cvt_pk_f16_f32 v2, v2, v3
	v_cvt_pk_f16_f32 v3, v6, v7
	v_pk_fma_f32 v[6:7], v[14:15], s[8:9], v[18:19] op_sel_hi:[1,0,1]
	v_pk_mul_f32 v[14:15], v[12:13], s[10:11] op_sel_hi:[1,0]
	v_pk_mul_f32 v[8:9], v[6:7], s[10:11] op_sel_hi:[1,0]
	ds_write2_b64 v23, v[4:5], v[2:3] offset1:2
	v_cvt_pk_f16_f32 v8, v8, v9
	v_cvt_pk_f16_f32 v9, v14, v15
	v_cvt_f32_f16_e32 v10, v8
	v_cvt_f32_f16_sdwa v11, v8 dst_sel:DWORD dst_unused:UNUSED_PAD src0_sel:WORD_1
	v_cvt_f32_f16_e32 v14, v9
	v_cvt_f32_f16_sdwa v15, v9 dst_sel:DWORD dst_unused:UNUSED_PAD src0_sel:WORD_1
	v_pk_fma_f32 v[2:3], v[6:7], s[10:11], v[10:11] op_sel_hi:[1,0,1] neg_lo:[0,0,1] neg_hi:[0,0,1]
	s_nop 0
	v_cvt_pk_f16_f32 v2, v2, v3
	v_pk_fma_f32 v[4:5], v[12:13], s[10:11], v[14:15] op_sel_hi:[1,0,1] neg_lo:[0,0,1] neg_hi:[0,0,1]
	s_nop 0
	v_cvt_pk_f16_f32 v3, v4, v5
	v_add_u32_e32 v4, v22, v40
	ds_write2_b64 v4, v[8:9], v[2:3] offset1:2
	v_lshl_add_u64 v[2:3], v[76:77], 0, s[6:7]
	s_waitcnt lgkmcnt(0)
	s_barrier
	global_load_dwordx4 v[66:69], v[2:3], off
	global_load_dwordx4 v[70:73], v[2:3], off offset:16
	s_lshl_b32 s12, s50, 5
	v_lshl_add_u64 v[10:11], s[12:13], 2, v[78:79]
	global_load_dwordx4 v[180:183], v[10:11], off
	global_load_dwordx4 v[184:187], v[10:11], off offset:32
	global_load_dwordx4 v[188:191], v[10:11], off offset:64
	global_load_dwordx4 v[192:195], v[10:11], off offset:96
	s_cmp_lt_u32 s5, 4
	s_cbranch_scc1 .Lvq_nosleep
	s_sleep 24
.Lvq_nosleep:
.LBB5_64:
	s_or_b32 s6, s15, s50
	s_lshl_b32 s12, s6, 5
	s_add_i32 s8, s6, 32
	s_mov_b32 s9, s13
	v_lshl_add_u64 v[10:11], s[12:13], 2, v[78:79]
	s_lshl_b64 s[8:9], s[8:9], 11
	global_load_dwordx4 v[196:199], v[10:11], off offset:128
	global_load_dwordx4 v[200:203], v[10:11], off offset:160
	global_load_dwordx4 v[204:207], v[10:11], off offset:192
	global_load_dwordx4 v[208:211], v[10:11], off offset:224
	v_lshl_add_u64 v[10:11], v[76:77], 0, s[8:9]
	global_load_dwordx4 v[100:103], v[10:11], off
	global_load_dwordx4 v[104:107], v[10:11], off offset:16
	ds_read_b128 v[34:37], v96
	ds_read_b128 v[38:41], v96 offset:16
	ds_read_b128 v[50:53], v96 offset:16896
	ds_read_b128 v[54:57], v96 offset:16912
	ds_read_b128 v[108:111], v96 offset:33792
	ds_read_b128 v[112:115], v96 offset:33808
	ds_read_b128 v[116:119], v96 offset:50688
	ds_read_b128 v[120:123], v96 offset:50704
	ds_read_b128 v[124:127], v96 offset:64
	ds_read_b128 v[128:131], v96 offset:80
	ds_read_b128 v[136:139], v96 offset:16960
	ds_read_b128 v[140:143], v96 offset:16976
	ds_read_b128 v[144:147], v96 offset:33856
	ds_read_b128 v[152:155], v96 offset:33872
	ds_read_b128 v[156:159], v96 offset:50752
	ds_read_b128 v[160:163], v96 offset:50768
	s_waitcnt vmcnt(6)
	v_pk_mul_f32 v[10:11], v[188:189], s[14:15] op_sel_hi:[1,0]
	v_pk_mul_f32 v[14:15], v[192:193], s[14:15] op_sel_hi:[1,0]
	v_pk_mul_f32 v[2:3], v[180:181], s[14:15] op_sel_hi:[1,0]
	v_pk_mul_f32 v[6:7], v[184:185], s[14:15] op_sel_hi:[1,0]
	v_pk_mul_f32 v[16:17], v[194:195], s[14:15] op_sel_hi:[1,0]
	v_pk_mul_f32 v[12:13], v[190:191], s[14:15] op_sel_hi:[1,0]
	v_pk_mul_f32 v[8:9], v[186:187], s[14:15] op_sel_hi:[1,0]
	v_pk_mul_f32 v[4:5], v[182:183], s[14:15] op_sel_hi:[1,0]
	s_waitcnt lgkmcnt(14)
	s_nop 0
	v_mfma_f32_32x32x16_f16 v[18:33], v[70:73], v[34:37], v[2:17]
	v_mfma_f32_32x32x16_f16 v[18:33], v[66:69], v[38:41], v[18:33]
	v_mfma_f32_32x32x16_f16 v[18:33], v[66:69], v[34:37], v[18:33]
	s_waitcnt lgkmcnt(13)
	v_mfma_f32_32x32x16_f16 v[34:49], v[70:73], v[50:53], v[2:17]
	s_waitcnt lgkmcnt(12)
	v_mfma_f32_32x32x16_f16 v[34:49], v[66:69], v[54:57], v[34:49]
	v_mfma_f32_32x32x16_f16 v[34:49], v[66:69], v[50:53], v[34:49]
	s_waitcnt lgkmcnt(11)
	v_mfma_f32_32x32x16_f16 v[50:65], v[70:73], v[108:111], v[2:17]
	s_waitcnt lgkmcnt(9)
	v_mfma_f32_32x32x16_f16 v[2:17], v[70:73], v[116:119], v[2:17]
	v_mfma_f32_32x32x16_f16 v[50:65], v[66:69], v[112:115], v[50:65]
	s_waitcnt lgkmcnt(8)
	v_mfma_f32_32x32x16_f16 v[2:17], v[66:69], v[120:123], v[2:17]
	v_mfma_f32_32x32x16_f16 v[50:65], v[66:69], v[108:111], v[50:65]
	v_mfma_f32_32x32x16_f16 v[2:17], v[66:69], v[116:119], v[2:17]
	s_add_i32 s8, s6, 64
	s_mov_b32 s9, s13
	s_lshl_b64 s[8:9], s[8:9], 11
	v_lshl_add_u64 v[70:71], v[76:77], 0, s[8:9]
	global_load_dwordx4 v[66:69], v[70:71], off
	s_nop 0
	global_load_dwordx4 v[70:73], v[70:71], off offset:16
	ds_read_b128 v[108:111], v96 offset:128
	ds_read_b128 v[112:115], v96 offset:144
	ds_read_b128 v[116:119], v96 offset:17024
	ds_read_b128 v[120:123], v96 offset:17040
	ds_read_b128 v[164:167], v96 offset:33920
	ds_read_b128 v[168:171], v96 offset:33936
	ds_read_b128 v[172:175], v96 offset:50816
	ds_read_b128 v[176:179], v96 offset:50832
	s_waitcnt vmcnt(2) lgkmcnt(14)
	v_mfma_f32_32x32x16_f16 v[18:33], v[104:107], v[124:127], v[18:33]
	s_waitcnt lgkmcnt(13)
	v_mfma_f32_32x32x16_f16 v[34:49], v[104:107], v[136:139], v[34:49]
	s_waitcnt lgkmcnt(11)
	v_mfma_f32_32x32x16_f16 v[50:65], v[104:107], v[144:147], v[50:65]
	s_waitcnt lgkmcnt(9)
	v_mfma_f32_32x32x16_f16 v[2:17], v[104:107], v[156:159], v[2:17]
	v_mfma_f32_32x32x16_f16 v[18:33], v[100:103], v[128:131], v[18:33]
	v_mfma_f32_32x32x16_f16 v[34:49], v[100:103], v[140:143], v[34:49]
	v_mfma_f32_32x32x16_f16 v[50:65], v[100:103], v[152:155], v[50:65]
	s_waitcnt lgkmcnt(8)
	v_mfma_f32_32x32x16_f16 v[2:17], v[100:103], v[160:163], v[2:17]
	v_mfma_f32_32x32x16_f16 v[18:33], v[100:103], v[124:127], v[18:33]
	v_mfma_f32_32x32x16_f16 v[34:49], v[100:103], v[136:139], v[34:49]
	v_mfma_f32_32x32x16_f16 v[50:65], v[100:103], v[144:147], v[50:65]
	v_mfma_f32_32x32x16_f16 v[2:17], v[100:103], v[156:159], v[2:17]
	s_add_i32 s8, s6, 0x60
	s_mov_b32 s9, s13
	s_lshl_b64 s[8:9], s[8:9], 11
	v_lshl_add_u64 v[104:105], v[76:77], 0, s[8:9]
	global_load_dwordx4 v[100:103], v[104:105], off
	s_nop 0
	global_load_dwordx4 v[104:107], v[104:105], off offset:16
	ds_read_b128 v[124:127], v96 offset:192
	ds_read_b128 v[128:131], v96 offset:208
	ds_read_b128 v[136:139], v96 offset:17088
	ds_read_b128 v[140:143], v96 offset:17104
	ds_read_b128 v[144:147], v96 offset:33984
	ds_read_b128 v[152:155], v96 offset:34000
	ds_read_b128 v[156:159], v96 offset:50880
	ds_read_b128 v[160:163], v96 offset:50896
	s_waitcnt vmcnt(2) lgkmcnt(14)
	v_mfma_f32_32x32x16_f16 v[18:33], v[70:73], v[108:111], v[18:33]
	s_waitcnt lgkmcnt(13)
	v_mfma_f32_32x32x16_f16 v[34:49], v[70:73], v[116:119], v[34:49]
	s_waitcnt lgkmcnt(11)
	v_mfma_f32_32x32x16_f16 v[50:65], v[70:73], v[164:167], v[50:65]
	s_waitcnt lgkmcnt(9)
	v_mfma_f32_32x32x16_f16 v[2:17], v[70:73], v[172:175], v[2:17]
	v_mfma_f32_32x32x16_f16 v[18:33], v[66:69], v[112:115], v[18:33]
	v_mfma_f32_32x32x16_f16 v[34:49], v[66:69], v[120:123], v[34:49]
	v_mfma_f32_32x32x16_f16 v[50:65], v[66:69], v[168:171], v[50:65]
	s_waitcnt lgkmcnt(8)
	v_mfma_f32_32x32x16_f16 v[2:17], v[66:69], v[176:179], v[2:17]
	v_mfma_f32_32x32x16_f16 v[18:33], v[66:69], v[108:111], v[18:33]
	v_mfma_f32_32x32x16_f16 v[34:49], v[66:69], v[116:119], v[34:49]
	v_mfma_f32_32x32x16_f16 v[50:65], v[66:69], v[164:167], v[50:65]
	v_mfma_f32_32x32x16_f16 v[2:17], v[66:69], v[172:175], v[2:17]
	s_add_i32 s8, s6, 0x80
	s_mov_b32 s9, s13
	s_lshl_b64 s[8:9], s[8:9], 11
	v_lshl_add_u64 v[70:71], v[76:77], 0, s[8:9]
	global_load_dwordx4 v[66:69], v[70:71], off
	s_nop 0
	global_load_dwordx4 v[70:73], v[70:71], off offset:16
	ds_read_b128 v[108:111], v96 offset:256
	ds_read_b128 v[112:115], v96 offset:272
	ds_read_b128 v[116:119], v96 offset:17152
	ds_read_b128 v[120:123], v96 offset:17168
	ds_read_b128 v[164:167], v96 offset:34048
	ds_read_b128 v[168:171], v96 offset:34064
	ds_read_b128 v[172:175], v96 offset:50944
	ds_read_b128 v[176:179], v96 offset:50960
	s_waitcnt vmcnt(2) lgkmcnt(14)
	v_mfma_f32_32x32x16_f16 v[18:33], v[104:107], v[124:127], v[18:33]
	s_waitcnt lgkmcnt(13)
	v_mfma_f32_32x32x16_f16 v[34:49], v[104:107], v[136:139], v[34:49]
	s_waitcnt lgkmcnt(11)
	v_mfma_f32_32x32x16_f16 v[50:65], v[104:107], v[144:147], v[50:65]
	s_waitcnt lgkmcnt(9)
	v_mfma_f32_32x32x16_f16 v[2:17], v[104:107], v[156:159], v[2:17]
	v_mfma_f32_32x32x16_f16 v[18:33], v[100:103], v[128:131], v[18:33]
	v_mfma_f32_32x32x16_f16 v[34:49], v[100:103], v[140:143], v[34:49]
	v_mfma_f32_32x32x16_f16 v[50:65], v[100:103], v[152:155], v[50:65]
	s_waitcnt lgkmcnt(8)
	v_mfma_f32_32x32x16_f16 v[2:17], v[100:103], v[160:163], v[2:17]
	v_mfma_f32_32x32x16_f16 v[18:33], v[100:103], v[124:127], v[18:33]
	v_mfma_f32_32x32x16_f16 v[34:49], v[100:103], v[136:139], v[34:49]
	v_mfma_f32_32x32x16_f16 v[50:65], v[100:103], v[144:147], v[50:65]
	v_mfma_f32_32x32x16_f16 v[2:17], v[100:103], v[156:159], v[2:17]
	s_add_i32 s8, s6, 0xa0
	s_mov_b32 s9, s13
	s_lshl_b64 s[8:9], s[8:9], 11
	v_lshl_add_u64 v[104:105], v[76:77], 0, s[8:9]
	global_load_dwordx4 v[100:103], v[104:105], off
	s_nop 0
	global_load_dwordx4 v[104:107], v[104:105], off offset:16
	ds_read_b128 v[124:127], v96 offset:320
	ds_read_b128 v[128:131], v96 offset:336
	ds_read_b128 v[136:139], v96 offset:17216
	ds_read_b128 v[140:143], v96 offset:17232
	ds_read_b128 v[144:147], v96 offset:34112
	ds_read_b128 v[152:155], v96 offset:34128
	ds_read_b128 v[156:159], v96 offset:51008
	ds_read_b128 v[160:163], v96 offset:51024
	s_waitcnt vmcnt(2) lgkmcnt(14)
	v_mfma_f32_32x32x16_f16 v[18:33], v[70:73], v[108:111], v[18:33]
	s_waitcnt lgkmcnt(13)
	v_mfma_f32_32x32x16_f16 v[34:49], v[70:73], v[116:119], v[34:49]
	s_waitcnt lgkmcnt(11)
	v_mfma_f32_32x32x16_f16 v[50:65], v[70:73], v[164:167], v[50:65]
	s_waitcnt lgkmcnt(9)
	v_mfma_f32_32x32x16_f16 v[2:17], v[70:73], v[172:175], v[2:17]
	v_mfma_f32_32x32x16_f16 v[18:33], v[66:69], v[112:115], v[18:33]
	v_mfma_f32_32x32x16_f16 v[34:49], v[66:69], v[120:123], v[34:49]
	v_mfma_f32_32x32x16_f16 v[50:65], v[66:69], v[168:171], v[50:65]
	s_waitcnt lgkmcnt(8)
	v_mfma_f32_32x32x16_f16 v[2:17], v[66:69], v[176:179], v[2:17]
	v_mfma_f32_32x32x16_f16 v[18:33], v[66:69], v[108:111], v[18:33]
	v_mfma_f32_32x32x16_f16 v[34:49], v[66:69], v[116:119], v[34:49]
	v_mfma_f32_32x32x16_f16 v[50:65], v[66:69], v[164:167], v[50:65]
	v_mfma_f32_32x32x16_f16 v[2:17], v[66:69], v[172:175], v[2:17]
	s_add_i32 s8, s6, 0xc0
	s_mov_b32 s9, s13
	s_lshl_b64 s[8:9], s[8:9], 11
	v_lshl_add_u64 v[70:71], v[76:77], 0, s[8:9]
	global_load_dwordx4 v[66:69], v[70:71], off
	s_nop 0
	global_load_dwordx4 v[70:73], v[70:71], off offset:16
	ds_read_b128 v[108:111], v96 offset:384
	ds_read_b128 v[112:115], v96 offset:400
	ds_read_b128 v[116:119], v96 offset:17280
	ds_read_b128 v[120:123], v96 offset:17296
	ds_read_b128 v[164:167], v96 offset:34176
	ds_read_b128 v[168:171], v96 offset:34192
	ds_read_b128 v[172:175], v96 offset:51072
	ds_read_b128 v[176:179], v96 offset:51088
	s_waitcnt vmcnt(2) lgkmcnt(14)
	v_mfma_f32_32x32x16_f16 v[18:33], v[104:107], v[124:127], v[18:33]
	s_waitcnt lgkmcnt(13)
	v_mfma_f32_32x32x16_f16 v[34:49], v[104:107], v[136:139], v[34:49]
	s_waitcnt lgkmcnt(11)
	v_mfma_f32_32x32x16_f16 v[50:65], v[104:107], v[144:147], v[50:65]
	s_waitcnt lgkmcnt(9)
	v_mfma_f32_32x32x16_f16 v[2:17], v[104:107], v[156:159], v[2:17]
	v_mfma_f32_32x32x16_f16 v[18:33], v[100:103], v[128:131], v[18:33]
	v_mfma_f32_32x32x16_f16 v[34:49], v[100:103], v[140:143], v[34:49]
	v_mfma_f32_32x32x16_f16 v[50:65], v[100:103], v[152:155], v[50:65]
	s_waitcnt lgkmcnt(8)
	v_mfma_f32_32x32x16_f16 v[2:17], v[100:103], v[160:163], v[2:17]
	v_mfma_f32_32x32x16_f16 v[18:33], v[100:103], v[124:127], v[18:33]
	v_mfma_f32_32x32x16_f16 v[34:49], v[100:103], v[136:139], v[34:49]
	v_mfma_f32_32x32x16_f16 v[50:65], v[100:103], v[144:147], v[50:65]
	v_mfma_f32_32x32x16_f16 v[2:17], v[100:103], v[156:159], v[2:17]
	s_add_i32 s8, s6, 0xe0
	s_mov_b32 s9, s13
	s_lshl_b64 s[8:9], s[8:9], 11
	v_lshl_add_u64 v[104:105], v[76:77], 0, s[8:9]
	global_load_dwordx4 v[100:103], v[104:105], off
	s_nop 0
	global_load_dwordx4 v[104:107], v[104:105], off offset:16
	ds_read_b128 v[124:127], v96 offset:448
	ds_read_b128 v[128:131], v96 offset:464
	ds_read_b128 v[136:139], v96 offset:17344
	ds_read_b128 v[140:143], v96 offset:17360
	ds_read_b128 v[144:147], v96 offset:34240
	ds_read_b128 v[152:155], v96 offset:34256
	ds_read_b128 v[156:159], v96 offset:51136
	ds_read_b128 v[160:163], v96 offset:51152
	s_waitcnt vmcnt(2) lgkmcnt(14)
	v_mfma_f32_32x32x16_f16 v[18:33], v[70:73], v[108:111], v[18:33]
	s_waitcnt lgkmcnt(13)
	v_mfma_f32_32x32x16_f16 v[34:49], v[70:73], v[116:119], v[34:49]
	s_waitcnt lgkmcnt(11)
	v_mfma_f32_32x32x16_f16 v[50:65], v[70:73], v[164:167], v[50:65]
	s_waitcnt lgkmcnt(9)
	v_mfma_f32_32x32x16_f16 v[2:17], v[70:73], v[172:175], v[2:17]
	v_mfma_f32_32x32x16_f16 v[18:33], v[66:69], v[112:115], v[18:33]
	v_mfma_f32_32x32x16_f16 v[34:49], v[66:69], v[120:123], v[34:49]
	v_mfma_f32_32x32x16_f16 v[50:65], v[66:69], v[168:171], v[50:65]
	s_waitcnt lgkmcnt(8)
	v_mfma_f32_32x32x16_f16 v[2:17], v[66:69], v[176:179], v[2:17]
	v_mfma_f32_32x32x16_f16 v[18:33], v[66:69], v[108:111], v[18:33]
	v_mfma_f32_32x32x16_f16 v[34:49], v[66:69], v[116:119], v[34:49]
	v_mfma_f32_32x32x16_f16 v[50:65], v[66:69], v[164:167], v[50:65]
	v_mfma_f32_32x32x16_f16 v[2:17], v[66:69], v[172:175], v[2:17]
	s_waitcnt vmcnt(0) lgkmcnt(7)
	v_mfma_f32_32x32x16_f16 v[18:33], v[104:107], v[124:127], v[18:33]
	s_waitcnt lgkmcnt(5)
	v_mfma_f32_32x32x16_f16 v[34:49], v[104:107], v[136:139], v[34:49]
	s_waitcnt lgkmcnt(3)
	v_mfma_f32_32x32x16_f16 v[50:65], v[104:107], v[144:147], v[50:65]
	s_waitcnt lgkmcnt(1)
	v_mfma_f32_32x32x16_f16 v[2:17], v[104:107], v[156:159], v[2:17]
	v_mfma_f32_32x32x16_f16 v[18:33], v[100:103], v[128:131], v[18:33]
	v_mfma_f32_32x32x16_f16 v[34:49], v[100:103], v[140:143], v[34:49]
	v_mfma_f32_32x32x16_f16 v[50:65], v[100:103], v[152:155], v[50:65]
	s_waitcnt lgkmcnt(0)
	v_mfma_f32_32x32x16_f16 v[2:17], v[100:103], v[160:163], v[2:17]
	v_mfma_f32_32x32x16_f16 v[18:33], v[100:103], v[124:127], v[18:33]
	v_mfma_f32_32x32x16_f16 v[34:49], v[100:103], v[136:139], v[34:49]
	v_mfma_f32_32x32x16_f16 v[50:65], v[100:103], v[144:147], v[50:65]
	v_mfma_f32_32x32x16_f16 v[2:17], v[100:103], v[156:159], v[2:17]
	s_add_i32 s6, s6, 1
	s_mov_b32 s7, s13
	s_nop 6
	v_max_f32_e32 v25, v25, v25
	v_max_f32_e32 v70, v24, v24
	v_max_f32_e32 v41, v41, v41
	v_max_f32_e32 v71, v40, v40
	s_lshl_b64 s[6:7], s[6:7], 11
	v_max_f32_e32 v21, v21, v21
	v_max_f32_e32 v66, v20, v20
	v_max_f32_e32 v37, v37, v37
	v_max_f32_e32 v67, v36, v36
	v_max_f32_e32 v53, v53, v53
	v_max_f32_e32 v68, v52, v52
	v_max_f32_e32 v5, v5, v5
	v_max_f32_e32 v69, v4, v4
	v_max_f32_e32 v57, v57, v57
	v_max_f32_e32 v72, v56, v56
	v_max_f32_e32 v9, v9, v9
	v_max_f32_e32 v73, v8, v8
	v_max_f32_e32 v25, v70, v25
	v_max_f32_e32 v41, v71, v41
	v_lshl_add_u64 v[70:71], v[76:77], 0, s[6:7]
	v_max_f32_e32 v21, v66, v21
	v_max_f32_e32 v37, v67, v37
	v_max_f32_e32 v53, v68, v53
	v_max_f32_e32 v5, v69, v5
	v_max_f32_e32 v57, v72, v57
	v_max_f32_e32 v9, v73, v9
	global_load_dwordx4 v[66:69], v[70:71], off
	s_nop 0
	global_load_dwordx4 v[70:73], v[70:71], off offset:16
	v_max3_f32 v21, v18, v19, v21
	v_max3_f32 v37, v34, v35, v37
	v_max3_f32 v53, v50, v51, v53
	v_max3_f32 v5, v2, v3, v5
	v_cmp_gt_f32_e32 vcc, v21, v98
	v_cmp_gt_f32_e64 s[6:7], v37, v93
	v_cmp_gt_f32_e64 s[8:9], v53, v89
	v_cmp_gt_f32_e64 s[10:11], v5, v85
	v_or_b32_e32 v99, s12, v134
	v_max_f32_e32 v29, v29, v29
	v_max_f32_e32 v100, v28, v28
	v_max_f32_e32 v45, v45, v45
	v_max_f32_e32 v101, v44, v44
	v_max_f32_e32 v61, v61, v61
	v_max_f32_e32 v102, v60, v60
	v_max_f32_e32 v13, v13, v13
	v_max_f32_e32 v103, v12, v12
	v_max3_f32 v25, v22, v23, v25
	v_max3_f32 v41, v38, v39, v41
	v_max3_f32 v57, v54, v55, v57
	v_max3_f32 v9, v6, v7, v9
	v_cndmask_b32_e32 v21, v98, v21, vcc
	v_cndmask_b32_e64 v37, v93, v37, s[6:7]
	v_cndmask_b32_e64 v53, v89, v53, s[8:9]
	v_cndmask_b32_e64 v5, v85, v5, s[10:11]
	v_max_f32_e32 v29, v100, v29
	v_max_f32_e32 v45, v101, v45
	v_max_f32_e32 v61, v102, v61
	v_max_f32_e32 v13, v103, v13
	v_cndmask_b32_e32 v81, v81, v99, vcc
	v_cndmask_b32_e32 v18, v97, v18, vcc
	v_cndmask_b32_e32 v19, v95, v19, vcc
	v_cndmask_b32_e32 v20, v94, v20, vcc
	v_cndmask_b32_e64 v80, v80, v99, s[6:7]
	v_cndmask_b32_e64 v34, v92, v34, s[6:7]
	v_cndmask_b32_e64 v35, v91, v35, s[6:7]
	v_cndmask_b32_e64 v36, v90, v36, s[6:7]
	v_cndmask_b32_e64 v74, v74, v99, s[8:9]
	v_cndmask_b32_e64 v50, v88, v50, s[8:9]
	v_cndmask_b32_e64 v51, v87, v51, s[8:9]
	v_cndmask_b32_e64 v52, v86, v52, s[8:9]
	v_cndmask_b32_e64 v75, v75, v99, s[10:11]
	v_cndmask_b32_e64 v2, v84, v2, s[10:11]
	v_cndmask_b32_e64 v3, v82, v3, s[10:11]
	v_cndmask_b32_e64 v4, v83, v4, s[10:11]
	v_cmp_gt_f32_e32 vcc, v25, v21
	v_cmp_gt_f32_e64 s[6:7], v41, v37
	v_cmp_gt_f32_e64 s[8:9], v57, v53
	v_cmp_gt_f32_e64 s[10:11], v9, v5
	v_max_f32_e32 v33, v33, v33
	v_max_f32_e32 v104, v32, v32
	v_max_f32_e32 v49, v49, v49
	v_max_f32_e32 v105, v48, v48
	v_max_f32_e32 v65, v65, v65
	v_max_f32_e32 v106, v64, v64
	v_max_f32_e32 v17, v17, v17
	v_max_f32_e32 v107, v16, v16
	v_add_u32_e32 v108, 8, v99
	v_max3_f32 v29, v26, v27, v29
	v_max3_f32 v45, v42, v43, v45
	v_max3_f32 v61, v58, v59, v61
	v_max3_f32 v13, v10, v11, v13
	v_cndmask_b32_e32 v21, v21, v25, vcc
	v_cndmask_b32_e64 v25, v37, v41, s[6:7]
	v_cndmask_b32_e64 v37, v53, v57, s[8:9]
	v_cndmask_b32_e64 v5, v5, v9, s[10:11]
	v_max_f32_e32 v33, v104, v33
	v_max_f32_e32 v49, v105, v49
	v_max_f32_e32 v65, v106, v65
	v_max_f32_e32 v17, v107, v17
	v_cndmask_b32_e32 v9, v81, v108, vcc
	v_cndmask_b32_e32 v18, v18, v22, vcc
	v_cndmask_b32_e32 v19, v19, v23, vcc
	v_cndmask_b32_e32 v20, v20, v24, vcc
	v_cndmask_b32_e64 v22, v80, v108, s[6:7]
	v_cndmask_b32_e64 v23, v34, v38, s[6:7]
	v_cndmask_b32_e64 v24, v35, v39, s[6:7]
	v_cndmask_b32_e64 v34, v36, v40, s[6:7]
	v_cndmask_b32_e64 v35, v74, v108, s[8:9]
	v_cndmask_b32_e64 v36, v50, v54, s[8:9]
	v_cndmask_b32_e64 v38, v51, v55, s[8:9]
	v_cndmask_b32_e64 v39, v52, v56, s[8:9]
	v_cndmask_b32_e64 v40, v75, v108, s[10:11]
	v_cndmask_b32_e64 v2, v2, v6, s[10:11]
	v_cndmask_b32_e64 v3, v3, v7, s[10:11]
	v_cndmask_b32_e64 v4, v4, v8, s[10:11]
	v_cmp_gt_f32_e32 vcc, v29, v21
	v_cmp_gt_f32_e64 s[6:7], v45, v25
	v_cmp_gt_f32_e64 s[8:9], v61, v37
	v_cmp_gt_f32_e64 s[10:11], v13, v5
	v_add_u32_e32 v109, 16, v99
	v_max3_f32 v33, v30, v31, v33
	v_max3_f32 v49, v46, v47, v49
	v_max3_f32 v65, v62, v63, v65
	v_max3_f32 v17, v14, v15, v17
	v_cndmask_b32_e32 v6, v21, v29, vcc
	v_cndmask_b32_e64 v7, v25, v45, s[6:7]
	v_cndmask_b32_e64 v8, v37, v61, s[8:9]
	v_cndmask_b32_e64 v5, v5, v13, s[10:11]
	s_add_i32 s15, s15, 1
	v_add_u32_e32 v100, 24, v99
	v_cndmask_b32_e32 v9, v9, v109, vcc
	v_cndmask_b32_e32 v13, v18, v26, vcc
	v_cndmask_b32_e32 v18, v19, v27, vcc
	v_cndmask_b32_e32 v19, v20, v28, vcc
	v_cndmask_b32_e64 v20, v22, v109, s[6:7]
	v_cndmask_b32_e64 v21, v23, v42, s[6:7]
	v_cndmask_b32_e64 v22, v24, v43, s[6:7]
	v_cndmask_b32_e64 v23, v34, v44, s[6:7]
	v_cndmask_b32_e64 v24, v35, v109, s[8:9]
	v_cndmask_b32_e64 v25, v36, v58, s[8:9]
	v_cndmask_b32_e64 v26, v38, v59, s[8:9]
	v_cndmask_b32_e64 v27, v39, v60, s[8:9]
	v_cndmask_b32_e64 v28, v40, v109, s[10:11]
	v_cndmask_b32_e64 v2, v2, v10, s[10:11]
	v_cndmask_b32_e64 v3, v3, v11, s[10:11]
	v_cndmask_b32_e64 v4, v4, v12, s[10:11]
	v_cmp_gt_f32_e32 vcc, v33, v6
	v_cmp_gt_f32_e64 s[6:7], v49, v7
	v_cmp_gt_f32_e64 s[8:9], v65, v8
	v_cmp_gt_f32_e64 s[10:11], v17, v5
	s_cmp_eq_u32 s15, 3
	v_cndmask_b32_e32 v98, v6, v33, vcc
	v_cndmask_b32_e64 v93, v7, v49, s[6:7]
	v_cndmask_b32_e64 v89, v8, v65, s[8:9]
	v_cndmask_b32_e64 v85, v5, v17, s[10:11]
	v_cndmask_b32_e32 v81, v9, v100, vcc
	v_cndmask_b32_e32 v97, v13, v30, vcc
	v_cndmask_b32_e32 v95, v18, v31, vcc
	v_cndmask_b32_e32 v94, v19, v32, vcc
	v_cndmask_b32_e64 v80, v20, v100, s[6:7]
	v_cndmask_b32_e64 v92, v21, v46, s[6:7]
	v_cndmask_b32_e64 v91, v22, v47, s[6:7]
	v_cndmask_b32_e64 v90, v23, v48, s[6:7]
	v_cndmask_b32_e64 v74, v24, v100, s[8:9]
	v_cndmask_b32_e64 v88, v25, v62, s[8:9]
	v_cndmask_b32_e64 v87, v26, v63, s[8:9]
	v_cndmask_b32_e64 v86, v27, v64, s[8:9]
	v_cndmask_b32_e64 v75, v28, v100, s[10:11]
	v_cndmask_b32_e64 v84, v2, v14, s[10:11]
	v_cndmask_b32_e64 v82, v3, v15, s[10:11]
	v_cndmask_b32_e64 v83, v4, v16, s[10:11]
	v_mov_b32_e32 v180, v196
	v_mov_b32_e32 v181, v197
	v_mov_b32_e32 v182, v198
	v_mov_b32_e32 v183, v199
	v_mov_b32_e32 v184, v200
	v_mov_b32_e32 v185, v201
	v_mov_b32_e32 v186, v202
	v_mov_b32_e32 v187, v203
	v_mov_b32_e32 v188, v204
	v_mov_b32_e32 v189, v205
	v_mov_b32_e32 v190, v206
	v_mov_b32_e32 v191, v207
	v_mov_b32_e32 v192, v208
	v_mov_b32_e32 v193, v209
	v_mov_b32_e32 v194, v210
	v_mov_b32_e32 v195, v211
	s_cbranch_scc0 .LBB5_64
	s_mov_b32 s53, 0
	s_lshl_b32 s52, s5, 7
	s_add_i32 s6, s50, 35
	s_mov_b32 s7, s53
	v_lshl_add_u64 v[10:11], s[52:53], 2, v[78:79]
	s_lshl_b64 s[6:7], s[6:7], 11
	v_lshl_add_u64 v[10:11], v[76:77], 0, s[6:7]
	global_load_dwordx4 v[100:103], v[10:11], off
	global_load_dwordx4 v[104:107], v[10:11], off offset:16
	ds_read_b128 v[24:27], v96
	ds_read_b128 v[28:31], v96 offset:16
	ds_read_b128 v[108:111], v96 offset:16896
	ds_read_b128 v[112:115], v96 offset:16912
	ds_read_b128 v[116:119], v96 offset:33792
	ds_read_b128 v[120:123], v96 offset:33808
	ds_read_b128 v[124:127], v96 offset:50688
	ds_read_b128 v[128:131], v96 offset:50704
	ds_read_b128 v[136:139], v96 offset:64
	ds_read_b128 v[140:143], v96 offset:80
	ds_read_b128 v[144:147], v96 offset:16960
	ds_read_b128 v[152:155], v96 offset:16976
	ds_read_b128 v[156:159], v96 offset:33856
	ds_read_b128 v[160:163], v96 offset:33872
	ds_read_b128 v[164:167], v96 offset:50752
	ds_read_b128 v[168:171], v96 offset:50768
	s_brev_b32 s6, 35
	s_waitcnt vmcnt(2)
	v_pk_mul_f32 v[10:11], v[188:189], s[6:7] op_sel_hi:[1,0]
	v_pk_mul_f32 v[14:15], v[192:193], s[6:7] op_sel_hi:[1,0]
	v_pk_mul_f32 v[2:3], v[180:181], s[6:7] op_sel_hi:[1,0]
	v_pk_mul_f32 v[6:7], v[184:185], s[6:7] op_sel_hi:[1,0]
	v_pk_mul_f32 v[16:17], v[194:195], s[6:7] op_sel_hi:[1,0]
	v_pk_mul_f32 v[12:13], v[190:191], s[6:7] op_sel_hi:[1,0]
	v_pk_mul_f32 v[8:9], v[186:187], s[6:7] op_sel_hi:[1,0]
	v_pk_mul_f32 v[4:5], v[182:183], s[6:7] op_sel_hi:[1,0]
	s_waitcnt lgkmcnt(14)
	s_nop 0
	v_mfma_f32_32x32x16_f16 v[50:65], v[70:73], v[24:27], v[2:17]
	v_mfma_f32_32x32x16_f16 v[50:65], v[66:69], v[28:31], v[50:65]
	v_mfma_f32_32x32x16_f16 v[50:65], v[66:69], v[24:27], v[50:65]
	s_waitcnt lgkmcnt(13)
	v_mfma_f32_32x32x16_f16 v[34:49], v[70:73], v[108:111], v[2:17]
	s_waitcnt lgkmcnt(11)
	v_mfma_f32_32x32x16_f16 v[18:33], v[70:73], v[116:119], v[2:17]
	s_waitcnt lgkmcnt(9)
	v_mfma_f32_32x32x16_f16 v[2:17], v[70:73], v[124:127], v[2:17]
	v_mfma_f32_32x32x16_f16 v[34:49], v[66:69], v[112:115], v[34:49]
	v_mfma_f32_32x32x16_f16 v[18:33], v[66:69], v[120:123], v[18:33]
	s_waitcnt lgkmcnt(8)
	v_mfma_f32_32x32x16_f16 v[2:17], v[66:69], v[128:131], v[2:17]
	v_mfma_f32_32x32x16_f16 v[34:49], v[66:69], v[108:111], v[34:49]
	v_mfma_f32_32x32x16_f16 v[18:33], v[66:69], v[116:119], v[18:33]
	v_mfma_f32_32x32x16_f16 v[2:17], v[66:69], v[124:127], v[2:17]
	s_add_i32 s6, s50, 0x43
	s_mov_b32 s7, s53
	s_lshl_b64 s[6:7], s[6:7], 11
	v_lshl_add_u64 v[70:71], v[76:77], 0, s[6:7]
	global_load_dwordx4 v[66:69], v[70:71], off
	s_nop 0
	global_load_dwordx4 v[70:73], v[70:71], off offset:16
	ds_read_b128 v[108:111], v96 offset:128
	ds_read_b128 v[112:115], v96 offset:144
	ds_read_b128 v[116:119], v96 offset:17024
	ds_read_b128 v[120:123], v96 offset:17040
	ds_read_b128 v[124:127], v96 offset:33920
	ds_read_b128 v[128:131], v96 offset:33936
	ds_read_b128 v[172:175], v96 offset:50816
	ds_read_b128 v[176:179], v96 offset:50832
	s_waitcnt vmcnt(2) lgkmcnt(14)
	v_mfma_f32_32x32x16_f16 v[50:65], v[104:107], v[136:139], v[50:65]
	s_waitcnt lgkmcnt(13)
	v_mfma_f32_32x32x16_f16 v[34:49], v[104:107], v[144:147], v[34:49]
	s_waitcnt lgkmcnt(11)
	v_mfma_f32_32x32x16_f16 v[18:33], v[104:107], v[156:159], v[18:33]
	s_waitcnt lgkmcnt(9)
	v_mfma_f32_32x32x16_f16 v[2:17], v[104:107], v[164:167], v[2:17]
	v_mfma_f32_32x32x16_f16 v[50:65], v[100:103], v[140:143], v[50:65]
	v_mfma_f32_32x32x16_f16 v[34:49], v[100:103], v[152:155], v[34:49]
	v_mfma_f32_32x32x16_f16 v[18:33], v[100:103], v[160:163], v[18:33]
	s_waitcnt lgkmcnt(8)
	v_mfma_f32_32x32x16_f16 v[2:17], v[100:103], v[168:171], v[2:17]
	v_mfma_f32_32x32x16_f16 v[50:65], v[100:103], v[136:139], v[50:65]
	v_mfma_f32_32x32x16_f16 v[34:49], v[100:103], v[144:147], v[34:49]
	v_mfma_f32_32x32x16_f16 v[18:33], v[100:103], v[156:159], v[18:33]
	v_mfma_f32_32x32x16_f16 v[2:17], v[100:103], v[164:167], v[2:17]
	s_add_i32 s6, s50, 0x63
	s_mov_b32 s7, s53
	s_lshl_b64 s[6:7], s[6:7], 11
	v_lshl_add_u64 v[78:79], v[76:77], 0, s[6:7]
	global_load_dwordx4 v[100:103], v[78:79], off
	global_load_dwordx4 v[104:107], v[78:79], off offset:16
	ds_read_b128 v[136:139], v96 offset:192
	ds_read_b128 v[140:143], v96 offset:208
	ds_read_b128 v[144:147], v96 offset:17088
	ds_read_b128 v[152:155], v96 offset:17104
	ds_read_b128 v[156:159], v96 offset:33984
	ds_read_b128 v[160:163], v96 offset:34000
	ds_read_b128 v[164:167], v96 offset:50880
	ds_read_b128 v[168:171], v96 offset:50896
	s_waitcnt vmcnt(2) lgkmcnt(14)
	v_mfma_f32_32x32x16_f16 v[50:65], v[70:73], v[108:111], v[50:65]
	s_waitcnt lgkmcnt(13)
	v_mfma_f32_32x32x16_f16 v[34:49], v[70:73], v[116:119], v[34:49]
	s_waitcnt lgkmcnt(11)
	v_mfma_f32_32x32x16_f16 v[18:33], v[70:73], v[124:127], v[18:33]
	s_waitcnt lgkmcnt(9)
	v_mfma_f32_32x32x16_f16 v[2:17], v[70:73], v[172:175], v[2:17]
	v_mfma_f32_32x32x16_f16 v[50:65], v[66:69], v[112:115], v[50:65]
	v_mfma_f32_32x32x16_f16 v[34:49], v[66:69], v[120:123], v[34:49]
	v_mfma_f32_32x32x16_f16 v[18:33], v[66:69], v[128:131], v[18:33]
	s_waitcnt lgkmcnt(8)
	v_mfma_f32_32x32x16_f16 v[2:17], v[66:69], v[176:179], v[2:17]
	v_mfma_f32_32x32x16_f16 v[50:65], v[66:69], v[108:111], v[50:65]
	v_mfma_f32_32x32x16_f16 v[34:49], v[66:69], v[116:119], v[34:49]
	v_mfma_f32_32x32x16_f16 v[18:33], v[66:69], v[124:127], v[18:33]
	v_mfma_f32_32x32x16_f16 v[2:17], v[66:69], v[172:175], v[2:17]
	s_add_i32 s6, s50, 0x83
	s_mov_b32 s7, s53
	s_lshl_b64 s[6:7], s[6:7], 11
	v_lshl_add_u64 v[70:71], v[76:77], 0, s[6:7]
	global_load_dwordx4 v[66:69], v[70:71], off
	s_nop 0
	global_load_dwordx4 v[70:73], v[70:71], off offset:16
	ds_read_b128 v[108:111], v96 offset:256
	ds_read_b128 v[112:115], v96 offset:272
	ds_read_b128 v[116:119], v96 offset:17152
	ds_read_b128 v[120:123], v96 offset:17168
	ds_read_b128 v[124:127], v96 offset:34048
	ds_read_b128 v[128:131], v96 offset:34064
	ds_read_b128 v[172:175], v96 offset:50944
	ds_read_b128 v[176:179], v96 offset:50960
	s_waitcnt vmcnt(2) lgkmcnt(14)
	v_mfma_f32_32x32x16_f16 v[50:65], v[104:107], v[136:139], v[50:65]
	s_waitcnt lgkmcnt(13)
	v_mfma_f32_32x32x16_f16 v[34:49], v[104:107], v[144:147], v[34:49]
	s_waitcnt lgkmcnt(11)
	v_mfma_f32_32x32x16_f16 v[18:33], v[104:107], v[156:159], v[18:33]
	s_waitcnt lgkmcnt(9)
	v_mfma_f32_32x32x16_f16 v[2:17], v[104:107], v[164:167], v[2:17]
	v_mfma_f32_32x32x16_f16 v[50:65], v[100:103], v[140:143], v[50:65]
	v_mfma_f32_32x32x16_f16 v[34:49], v[100:103], v[152:155], v[34:49]
	v_mfma_f32_32x32x16_f16 v[18:33], v[100:103], v[160:163], v[18:33]
	s_waitcnt lgkmcnt(8)
	v_mfma_f32_32x32x16_f16 v[2:17], v[100:103], v[168:171], v[2:17]
	v_mfma_f32_32x32x16_f16 v[50:65], v[100:103], v[136:139], v[50:65]
	v_mfma_f32_32x32x16_f16 v[34:49], v[100:103], v[144:147], v[34:49]
	v_mfma_f32_32x32x16_f16 v[18:33], v[100:103], v[156:159], v[18:33]
	v_mfma_f32_32x32x16_f16 v[2:17], v[100:103], v[164:167], v[2:17]
	s_add_i32 s6, s50, 0xa3
	s_mov_b32 s7, s53
	s_lshl_b64 s[6:7], s[6:7], 11
	v_lshl_add_u64 v[78:79], v[76:77], 0, s[6:7]
	global_load_dwordx4 v[100:103], v[78:79], off
	global_load_dwordx4 v[104:107], v[78:79], off offset:16
	ds_read_b128 v[136:139], v96 offset:320
	ds_read_b128 v[140:143], v96 offset:336
	ds_read_b128 v[144:147], v96 offset:17216
	ds_read_b128 v[152:155], v96 offset:17232
	ds_read_b128 v[156:159], v96 offset:34112
	ds_read_b128 v[160:163], v96 offset:34128
	ds_read_b128 v[164:167], v96 offset:51008
	ds_read_b128 v[168:171], v96 offset:51024
	s_waitcnt vmcnt(2) lgkmcnt(14)
	v_mfma_f32_32x32x16_f16 v[50:65], v[70:73], v[108:111], v[50:65]
	s_waitcnt lgkmcnt(13)
	v_mfma_f32_32x32x16_f16 v[34:49], v[70:73], v[116:119], v[34:49]
	s_waitcnt lgkmcnt(11)
	v_mfma_f32_32x32x16_f16 v[18:33], v[70:73], v[124:127], v[18:33]
	s_waitcnt lgkmcnt(9)
	v_mfma_f32_32x32x16_f16 v[2:17], v[70:73], v[172:175], v[2:17]
	v_mfma_f32_32x32x16_f16 v[50:65], v[66:69], v[112:115], v[50:65]
	v_mfma_f32_32x32x16_f16 v[34:49], v[66:69], v[120:123], v[34:49]
	v_mfma_f32_32x32x16_f16 v[18:33], v[66:69], v[128:131], v[18:33]
	s_waitcnt lgkmcnt(8)
	v_mfma_f32_32x32x16_f16 v[2:17], v[66:69], v[176:179], v[2:17]
	v_mfma_f32_32x32x16_f16 v[50:65], v[66:69], v[108:111], v[50:65]
	v_mfma_f32_32x32x16_f16 v[34:49], v[66:69], v[116:119], v[34:49]
	v_mfma_f32_32x32x16_f16 v[18:33], v[66:69], v[124:127], v[18:33]
	v_mfma_f32_32x32x16_f16 v[2:17], v[66:69], v[172:175], v[2:17]
	s_add_i32 s6, s50, 0xc3
	s_mov_b32 s7, s53
	s_lshl_b64 s[6:7], s[6:7], 11
	v_lshl_add_u64 v[70:71], v[76:77], 0, s[6:7]
	global_load_dwordx4 v[66:69], v[70:71], off
	s_nop 0
	global_load_dwordx4 v[70:73], v[70:71], off offset:16
	ds_read_b128 v[108:111], v96 offset:384
	ds_read_b128 v[112:115], v96 offset:400
	ds_read_b128 v[116:119], v96 offset:17280
	ds_read_b128 v[120:123], v96 offset:17296
	ds_read_b128 v[124:127], v96 offset:34176
	ds_read_b128 v[128:131], v96 offset:34192
	ds_read_b128 v[172:175], v96 offset:51072
	ds_read_b128 v[176:179], v96 offset:51088
	s_waitcnt vmcnt(2) lgkmcnt(14)
	v_mfma_f32_32x32x16_f16 v[50:65], v[104:107], v[136:139], v[50:65]
	s_waitcnt lgkmcnt(13)
	v_mfma_f32_32x32x16_f16 v[34:49], v[104:107], v[144:147], v[34:49]
	s_waitcnt lgkmcnt(11)
	v_mfma_f32_32x32x16_f16 v[18:33], v[104:107], v[156:159], v[18:33]
	s_waitcnt lgkmcnt(9)
	v_mfma_f32_32x32x16_f16 v[2:17], v[104:107], v[164:167], v[2:17]
	v_mfma_f32_32x32x16_f16 v[50:65], v[100:103], v[140:143], v[50:65]
	v_mfma_f32_32x32x16_f16 v[34:49], v[100:103], v[152:155], v[34:49]
	v_mfma_f32_32x32x16_f16 v[18:33], v[100:103], v[160:163], v[18:33]
	s_waitcnt lgkmcnt(8)
	v_mfma_f32_32x32x16_f16 v[2:17], v[100:103], v[168:171], v[2:17]
	v_mfma_f32_32x32x16_f16 v[50:65], v[100:103], v[136:139], v[50:65]
	v_mfma_f32_32x32x16_f16 v[34:49], v[100:103], v[144:147], v[34:49]
	v_mfma_f32_32x32x16_f16 v[18:33], v[100:103], v[156:159], v[18:33]
	v_mfma_f32_32x32x16_f16 v[2:17], v[100:103], v[164:167], v[2:17]
	s_add_i32 s6, s50, 0xe3
	s_mov_b32 s7, s53
	s_lshl_b64 s[6:7], s[6:7], 11
	v_lshl_add_u64 v[100:101], v[76:77], 0, s[6:7]
	global_load_dwordx4 v[76:79], v[100:101], off
	s_nop 0
	global_load_dwordx4 v[100:103], v[100:101], off offset:16
	ds_read_b128 v[104:107], v96 offset:448
	ds_read_b128 v[136:139], v96 offset:464
	ds_read_b128 v[140:143], v96 offset:17344
	ds_read_b128 v[144:147], v96 offset:17360
	ds_read_b128 v[152:155], v96 offset:34240
	ds_read_b128 v[156:159], v96 offset:34256
	ds_read_b128 v[160:163], v96 offset:51136
	ds_read_b128 v[164:167], v96 offset:51152
	s_waitcnt vmcnt(2) lgkmcnt(14)
	v_mfma_f32_32x32x16_f16 v[50:65], v[70:73], v[108:111], v[50:65]
	s_waitcnt lgkmcnt(13)
	v_mfma_f32_32x32x16_f16 v[34:49], v[70:73], v[116:119], v[34:49]
	s_waitcnt lgkmcnt(11)
	v_mfma_f32_32x32x16_f16 v[18:33], v[70:73], v[124:127], v[18:33]
	s_waitcnt lgkmcnt(9)
	v_mfma_f32_32x32x16_f16 v[2:17], v[70:73], v[172:175], v[2:17]
	v_mfma_f32_32x32x16_f16 v[50:65], v[66:69], v[112:115], v[50:65]
	v_mfma_f32_32x32x16_f16 v[34:49], v[66:69], v[120:123], v[34:49]
	v_mfma_f32_32x32x16_f16 v[18:33], v[66:69], v[128:131], v[18:33]
	s_waitcnt lgkmcnt(8)
	v_mfma_f32_32x32x16_f16 v[2:17], v[66:69], v[176:179], v[2:17]
	v_mfma_f32_32x32x16_f16 v[50:65], v[66:69], v[108:111], v[50:65]
	v_mfma_f32_32x32x16_f16 v[34:49], v[66:69], v[116:119], v[34:49]
	v_mfma_f32_32x32x16_f16 v[18:33], v[66:69], v[124:127], v[18:33]
	v_mfma_f32_32x32x16_f16 v[2:17], v[66:69], v[172:175], v[2:17]
	s_waitcnt vmcnt(0) lgkmcnt(7)
	v_mfma_f32_32x32x16_f16 v[50:65], v[100:103], v[104:107], v[50:65]
	s_waitcnt lgkmcnt(5)
	v_mfma_f32_32x32x16_f16 v[34:49], v[100:103], v[140:143], v[34:49]
	s_waitcnt lgkmcnt(3)
	v_mfma_f32_32x32x16_f16 v[18:33], v[100:103], v[152:155], v[18:33]
	s_waitcnt lgkmcnt(1)
	v_mfma_f32_32x32x16_f16 v[2:17], v[100:103], v[160:163], v[2:17]
	v_mfma_f32_32x32x16_f16 v[50:65], v[76:79], v[136:139], v[50:65]
	v_mfma_f32_32x32x16_f16 v[34:49], v[76:79], v[144:147], v[34:49]
	v_mfma_f32_32x32x16_f16 v[18:33], v[76:79], v[156:159], v[18:33]
	s_waitcnt lgkmcnt(0)
	v_mfma_f32_32x32x16_f16 v[2:17], v[76:79], v[164:167], v[2:17]
	v_mfma_f32_32x32x16_f16 v[50:65], v[76:79], v[104:107], v[50:65]
	v_mfma_f32_32x32x16_f16 v[34:49], v[76:79], v[140:143], v[34:49]
	v_mfma_f32_32x32x16_f16 v[18:33], v[76:79], v[152:155], v[18:33]
	v_mfma_f32_32x32x16_f16 v[2:17], v[76:79], v[160:163], v[2:17]
	s_nop 8
	v_max_f32_e32 v53, v53, v53
	v_max_f32_e32 v66, v52, v52
	v_max_f32_e32 v53, v66, v53
	v_max3_f32 v53, v50, v51, v53
	v_max_f32_e32 v57, v57, v57
	v_max_f32_e32 v66, v56, v56
	v_cmp_gt_f32_e64 s[36:37], v53, v98
	v_max_f32_e32 v57, v66, v57
	v_max3_f32 v57, v54, v55, v57
	v_cndmask_b32_e64 v53, v98, v53, s[36:37]
	v_cndmask_b32_e64 v50, v97, v50, s[36:37]
	v_cmp_gt_f32_e64 s[8:9], v57, v53
	s_nop 1
	v_cndmask_b32_e64 v53, v53, v57, s[8:9]
	v_cndmask_b32_e64 v50, v50, v54, s[8:9]
	v_max_f32_e32 v54, v61, v61
	v_max_f32_e32 v57, v60, v60
	v_max_f32_e32 v54, v57, v54
	v_max3_f32 v54, v58, v59, v54
	v_cmp_gt_f32_e64 s[14:15], v54, v53
	v_max_f32_e32 v57, v64, v64
	s_nop 0
	v_cndmask_b32_e64 v53, v53, v54, s[14:15]
	v_max_f32_e32 v54, v65, v65
	v_max_f32_e32 v54, v57, v54
	v_max3_f32 v54, v62, v63, v54
	v_cndmask_b32_e64 v50, v50, v58, s[14:15]
	v_cmp_gt_f32_e64 s[20:21], v54, v53
	s_nop 1
	v_cndmask_b32_e64 v53, v53, v54, s[20:21]
	v_cndmask_b32_e64 v50, v50, v62, s[20:21]
	v_cmp_neq_f32_e32 vcc, v50, v53
	v_mov_b32_e32 v50, 0
	v_mov_b32_e32 v54, 0
	s_and_saveexec_b64 s[6:7], vcc
	s_cbranch_execz .LBB5_69
	v_cndmask_b32_e64 v51, v95, v51, s[36:37]
	v_cndmask_b32_e64 v51, v51, v55, s[8:9]
	v_cndmask_b32_e64 v51, v51, v59, s[14:15]
	v_cndmask_b32_e64 v51, v51, v63, s[20:21]
	v_cmp_neq_f32_e32 vcc, v51, v53
	v_mov_b32_e32 v54, 1
	s_and_saveexec_b64 s[10:11], vcc
	v_cndmask_b32_e64 v51, v94, v52, s[36:37]
	v_cndmask_b32_e64 v51, v51, v56, s[8:9]
	v_cndmask_b32_e64 v51, v51, v60, s[14:15]
	v_cndmask_b32_e64 v51, v51, v64, s[20:21]
	v_cmp_eq_f32_e32 vcc, v51, v53
	s_nop 1
	v_cndmask_b32_e64 v54, 3, 2, vcc
	s_or_b64 exec, exec, s[10:11]
